# baseline (speedup 1.0000x reference)
.LBB1_16:
	s_or_b64 exec, exec, s[10:11]
	s_or_b32 s32, s28, 8
	s_mov_b32 s33, 0
	s_lshl_b64 s[32:33], s[32:33], 12
	v_lshl_add_u64 v[112:113], v[96:97], 0, s[32:33]
	global_load_dwordx4 v[110:113], v[112:113], off nt
	v_cvt_f64_f32_e32 v[16:17], v16
	v_cvt_f64_f32_e32 v[14:15], v10
	v_mul_f64 v[20:21], v[52:53], v[16:17]
	v_mul_f64 v[28:29], v[42:43], v[16:17]
	v_cvt_f64_f32_e32 v[10:11], v11
	v_fmac_f64_e32 v[20:21], v[48:49], v[14:15]
	v_fmac_f64_e32 v[28:29], v[36:37], v[14:15]
	s_waitcnt lgkmcnt(0)
	v_cvt_f64_f32_e32 v[18:19], v13
	v_fmac_f64_e32 v[20:21], v[50:51], v[10:11]
	v_fmac_f64_e32 v[28:29], v[38:39], v[10:11]
	v_fmac_f64_e32 v[20:21], v[46:47], v[18:19]
	v_mul_f64 v[22:23], v[74:75], v[16:17]
	v_fmac_f64_e32 v[28:29], v[34:35], v[18:19]
	v_mul_f64 v[98:99], v[44:45], v[16:17]
	v_fmac_f64_e32 v[22:23], v[64:65], v[14:15]
	v_mul_f64 v[24:25], v[84:85], v[16:17]
	v_mul_f64 v[26:27], v[92:93], v[16:17]
	v_fmac_f64_e32 v[98:99], v[32:33], v[14:15]
	v_mul_f64 v[102:103], v[60:61], v[16:17]
	v_mul_f64 v[16:17], v[76:77], v[16:17]
	v_cndmask_b32_e32 v3, v21, v29, vcc
	v_cndmask_b32_e32 v4, v20, v28, vcc
	v_fmac_f64_e32 v[22:23], v[66:67], v[10:11]
	v_fmac_f64_e32 v[24:25], v[80:81], v[14:15]
	v_fmac_f64_e32 v[26:27], v[88:89], v[14:15]
	v_fmac_f64_e32 v[98:99], v[40:41], v[10:11]
	v_fmac_f64_e32 v[102:103], v[56:57], v[14:15]
	v_fmac_f64_e32 v[16:17], v[70:71], v[14:15]
	ds_bpermute_b32 v14, v101, v4
	ds_bpermute_b32 v15, v101, v3
	v_fmac_f64_e32 v[22:23], v[62:63], v[18:19]
	v_fmac_f64_e32 v[24:25], v[82:83], v[10:11]
	v_fmac_f64_e32 v[98:99], v[30:31], v[18:19]
	v_fmac_f64_e32 v[102:103], v[58:59], v[10:11]
	v_fmac_f64_e32 v[24:25], v[78:79], v[18:19]
	v_fmac_f64_e32 v[26:27], v[90:91], v[10:11]
	v_fmac_f64_e32 v[102:103], v[54:55], v[18:19]
	v_fmac_f64_e32 v[16:17], v[72:73], v[10:11]
	v_cndmask_b32_e32 v3, v23, v99, vcc
	v_cndmask_b32_e32 v4, v22, v98, vcc
	v_fmac_f64_e32 v[26:27], v[86:87], v[18:19]
	v_fmac_f64_e32 v[16:17], v[68:69], v[18:19]
	ds_bpermute_b32 v18, v101, v4
	ds_bpermute_b32 v19, v101, v3
	v_cndmask_b32_e32 v3, v25, v103, vcc
	v_cndmask_b32_e32 v4, v24, v102, vcc
	v_cndmask_b32_e32 v11, v29, v21, vcc
	v_cndmask_b32_e32 v10, v28, v20, vcc
	ds_bpermute_b32 v20, v101, v4
	ds_bpermute_b32 v21, v101, v3
	v_cndmask_b32_e32 v3, v27, v17, vcc
	v_cndmask_b32_e32 v4, v26, v16, vcc
	s_waitcnt lgkmcnt(4)
	v_add_f64 v[10:11], v[10:11], v[14:15]
	v_cndmask_b32_e32 v15, v99, v23, vcc
	v_cndmask_b32_e32 v14, v98, v22, vcc
	ds_bpermute_b32 v22, v101, v4
	ds_bpermute_b32 v23, v101, v3
	s_waitcnt lgkmcnt(4)
	v_add_f64 v[14:15], v[14:15], v[18:19]
	v_cndmask_b32_e32 v19, v103, v25, vcc
	v_cndmask_b32_e32 v18, v102, v24, vcc
	s_waitcnt lgkmcnt(2)
	v_add_f64 v[18:19], v[18:19], v[20:21]
	v_cndmask_b32_e32 v17, v17, v27, vcc
	v_cndmask_b32_e32 v16, v16, v26, vcc
	s_waitcnt lgkmcnt(0)
	v_add_f64 v[16:17], v[16:17], v[22:23]
	v_cndmask_b32_e64 v3, v11, v19, s[8:9]
	v_cndmask_b32_e64 v4, v10, v18, s[8:9]
	ds_bpermute_b32 v20, v104, v4
	ds_bpermute_b32 v21, v104, v3
	v_cndmask_b32_e64 v3, v15, v17, s[8:9]
	v_cndmask_b32_e64 v4, v14, v16, s[8:9]
	ds_bpermute_b32 v22, v104, v4
	ds_bpermute_b32 v23, v104, v3
	v_cndmask_b32_e64 v11, v19, v11, s[8:9]
	v_cndmask_b32_e64 v10, v18, v10, s[8:9]
	v_cndmask_b32_e64 v15, v17, v15, s[8:9]
	v_cndmask_b32_e64 v14, v16, v14, s[8:9]
	s_waitcnt lgkmcnt(2)
	v_add_f64 v[10:11], v[10:11], v[20:21]
	s_waitcnt lgkmcnt(0)
	v_add_f64 v[14:15], v[14:15], v[22:23]
	v_cndmask_b32_e64 v3, v11, v15, s[4:5]
	v_cndmask_b32_e64 v4, v10, v14, s[4:5]
	ds_bpermute_b32 v16, v105, v4
	ds_bpermute_b32 v17, v105, v3
	v_cndmask_b32_e64 v11, v15, v11, s[4:5]
	v_cndmask_b32_e64 v10, v14, v10, s[4:5]
	s_waitcnt lgkmcnt(0)
	v_add_f64 v[10:11], v[10:11], v[16:17]
	ds_bpermute_b32 v14, v106, v10
	ds_bpermute_b32 v15, v106, v11
	s_waitcnt lgkmcnt(0)
	v_add_f64 v[10:11], v[10:11], v[14:15]
	ds_bpermute_b32 v14, v107, v10
	ds_bpermute_b32 v15, v107, v11
	s_waitcnt lgkmcnt(0)
	v_add_f64 v[10:11], v[10:11], v[14:15]
	ds_bpermute_b32 v14, v109, v10
	ds_bpermute_b32 v15, v109, v11
	s_and_saveexec_b64 s[10:11], s[6:7]
	s_cbranch_execz .LBB1_18
	s_waitcnt lgkmcnt(0)
	v_add_f64 v[10:11], v[10:11], v[14:15]
	ds_write_b64 v108, v[10:11] offset:1280

.LBB1_20:
	s_or_b64 exec, exec, s[10:11]
	s_or_b32 s32, s28, 9
	s_mov_b32 s33, 0
	s_lshl_b64 s[32:33], s[32:33], 12
	v_lshl_add_u64 v[28:29], v[96:97], 0, s[32:33]
	global_load_dwordx4 v[26:29], v[28:29], off nt
	v_cvt_f64_f32_e32 v[6:7], v8
	v_cvt_f64_f32_e32 v[2:3], v2
	s_waitcnt lgkmcnt(0)
	v_mul_f64 v[10:11], v[52:53], v[6:7]
	v_mul_f64 v[18:19], v[42:43], v[6:7]
	v_cvt_f64_f32_e32 v[8:9], v1
	v_fmac_f64_e32 v[10:11], v[48:49], v[2:3]
	v_mul_f64 v[12:13], v[74:75], v[6:7]
	v_fmac_f64_e32 v[18:19], v[36:37], v[2:3]
	v_mul_f64 v[20:21], v[44:45], v[6:7]
	v_cvt_f64_f32_e32 v[4:5], v5
	v_fmac_f64_e32 v[10:11], v[50:51], v[8:9]
	v_fmac_f64_e32 v[12:13], v[64:65], v[2:3]
	v_mul_f64 v[14:15], v[84:85], v[6:7]
	v_mul_f64 v[16:17], v[92:93], v[6:7]
	v_fmac_f64_e32 v[18:19], v[38:39], v[8:9]
	v_fmac_f64_e32 v[20:21], v[32:33], v[2:3]
	v_mul_f64 v[22:23], v[60:61], v[6:7]
	v_mul_f64 v[6:7], v[76:77], v[6:7]
	v_fmac_f64_e32 v[10:11], v[46:47], v[4:5]
	v_fmac_f64_e32 v[12:13], v[66:67], v[8:9]
	v_fmac_f64_e32 v[14:15], v[80:81], v[2:3]
	v_fmac_f64_e32 v[16:17], v[88:89], v[2:3]
	v_fmac_f64_e32 v[18:19], v[34:35], v[4:5]
	v_fmac_f64_e32 v[20:21], v[40:41], v[8:9]
	v_fmac_f64_e32 v[22:23], v[56:57], v[2:3]
	v_fmac_f64_e32 v[6:7], v[70:71], v[2:3]
	v_fmac_f64_e32 v[12:13], v[62:63], v[4:5]
	v_fmac_f64_e32 v[14:15], v[82:83], v[8:9]
	v_fmac_f64_e32 v[16:17], v[90:91], v[8:9]
	v_fmac_f64_e32 v[20:21], v[30:31], v[4:5]
	v_fmac_f64_e32 v[22:23], v[58:59], v[8:9]
	v_fmac_f64_e32 v[6:7], v[72:73], v[8:9]
	v_cndmask_b32_e32 v1, v11, v19, vcc
	v_cndmask_b32_e32 v2, v10, v18, vcc
	v_fmac_f64_e32 v[14:15], v[78:79], v[4:5]
	v_fmac_f64_e32 v[16:17], v[86:87], v[4:5]
	v_fmac_f64_e32 v[22:23], v[54:55], v[4:5]
	v_fmac_f64_e32 v[6:7], v[68:69], v[4:5]
	ds_bpermute_b32 v4, v101, v2
	ds_bpermute_b32 v5, v101, v1
	v_cndmask_b32_e32 v1, v13, v21, vcc
	v_cndmask_b32_e32 v2, v12, v20, vcc
	ds_bpermute_b32 v8, v101, v2
	ds_bpermute_b32 v9, v101, v1
	v_cndmask_b32_e32 v3, v19, v11, vcc
	v_cndmask_b32_e32 v2, v18, v10, vcc
	s_waitcnt lgkmcnt(2)
	v_add_f64 v[2:3], v[2:3], v[4:5]
	v_cndmask_b32_e32 v5, v21, v13, vcc
	v_cndmask_b32_e32 v4, v20, v12, vcc
	s_waitcnt lgkmcnt(0)
	v_add_f64 v[4:5], v[4:5], v[8:9]
	v_cndmask_b32_e32 v1, v15, v23, vcc
	v_cndmask_b32_e32 v8, v14, v22, vcc
	ds_bpermute_b32 v10, v101, v8
	ds_bpermute_b32 v11, v101, v1
	v_cndmask_b32_e32 v1, v17, v7, vcc
	v_cndmask_b32_e32 v8, v16, v6, vcc
	ds_bpermute_b32 v12, v101, v8
	ds_bpermute_b32 v13, v101, v1
	v_cndmask_b32_e32 v9, v23, v15, vcc
	v_cndmask_b32_e32 v8, v22, v14, vcc
	s_waitcnt lgkmcnt(2)
	v_add_f64 v[8:9], v[8:9], v[10:11]
	v_cndmask_b32_e32 v7, v7, v17, vcc
	v_cndmask_b32_e32 v6, v6, v16, vcc
	s_waitcnt lgkmcnt(0)
	v_add_f64 v[6:7], v[6:7], v[12:13]
	v_cndmask_b32_e64 v1, v3, v9, s[8:9]
	v_cndmask_b32_e64 v10, v2, v8, s[8:9]
	v_cndmask_b32_e64 v3, v9, v3, s[8:9]
	ds_bpermute_b32 v11, v104, v1
	v_cndmask_b32_e64 v1, v5, v7, s[8:9]
	v_cndmask_b32_e64 v9, v4, v6, s[8:9]
	ds_bpermute_b32 v10, v104, v10
	ds_bpermute_b32 v12, v104, v9
	ds_bpermute_b32 v13, v104, v1
	v_cndmask_b32_e64 v2, v8, v2, s[8:9]
	v_cndmask_b32_e64 v5, v7, v5, s[8:9]
	v_cndmask_b32_e64 v4, v6, v4, s[8:9]
	s_waitcnt lgkmcnt(2)
	v_add_f64 v[2:3], v[2:3], v[10:11]
	s_waitcnt lgkmcnt(0)
	v_add_f64 v[4:5], v[4:5], v[12:13]
	v_cndmask_b32_e64 v1, v3, v5, s[4:5]
	v_cndmask_b32_e64 v6, v2, v4, s[4:5]
	ds_bpermute_b32 v6, v105, v6
	ds_bpermute_b32 v7, v105, v1
	v_cndmask_b32_e64 v3, v5, v3, s[4:5]
	v_cndmask_b32_e64 v2, v4, v2, s[4:5]
	s_waitcnt lgkmcnt(0)
	v_add_f64 v[2:3], v[2:3], v[6:7]
	ds_bpermute_b32 v4, v106, v2
	ds_bpermute_b32 v5, v106, v3
	s_waitcnt lgkmcnt(0)
	v_add_f64 v[2:3], v[2:3], v[4:5]
	ds_bpermute_b32 v4, v107, v2
	ds_bpermute_b32 v5, v107, v3
	s_waitcnt lgkmcnt(0)
	v_add_f64 v[2:3], v[2:3], v[4:5]
	ds_bpermute_b32 v4, v109, v2
	ds_bpermute_b32 v5, v109, v3
	s_and_saveexec_b64 s[10:11], s[6:7]
	s_cbranch_execz .LBB1_22
	s_waitcnt lgkmcnt(0)
	v_add_f64 v[2:3], v[2:3], v[4:5]
	ds_write_b64 v108, v[2:3] offset:1792
.LBB1_22:
	s_or_b64 exec, exec, s[10:11]
	s_or_b32 s14, s28, 8
	s_mov_b32 s15, 0
	s_lshl_b64 s[10:11], s[14:15], 12
	v_lshl_add_u64 v[2:3], v[96:97], 0, s[10:11]
	s_or_b32 s16, s28, 9
	s_mov_b32 s17, s15
	s_lshl_b64 s[10:11], s[16:17], 12
	v_lshl_add_u64 v[2:3], v[96:97], 0, s[10:11]
	s_or_b32 s18, s28, 10
	s_mov_b32 s19, s15
	s_lshl_b64 s[10:11], s[18:19], 12
	s_or_b32 s20, s28, 11
	s_mov_b32 s21, s15
	v_lshl_add_u64 v[2:3], v[96:97], 0, s[10:11]
	s_lshl_b64 s[10:11], s[20:21], 12
	global_load_dwordx4 v[22:25], v[2:3], off nt
	v_lshl_add_u64 v[2:3], v[96:97], 0, s[10:11]
	global_load_dwordx4 v[18:21], v[2:3], off nt
	s_or_b32 s22, s28, 12
	s_mov_b32 s23, s15
	s_lshl_b64 s[10:11], s[22:23], 12
	s_or_b32 s24, s28, 13
	s_mov_b32 s25, s15
	v_lshl_add_u64 v[2:3], v[96:97], 0, s[10:11]
	s_lshl_b64 s[10:11], s[24:25], 12
	global_load_dwordx4 v[14:17], v[2:3], off nt
	v_lshl_add_u64 v[2:3], v[96:97], 0, s[10:11]
	global_load_dwordx4 v[10:13], v[2:3], off nt
	s_or_b32 s12, s28, 14
	s_mov_b32 s13, s15
	s_lshl_b64 s[10:11], s[12:13], 12
	v_lshl_add_u64 v[2:3], v[96:97], 0, s[10:11]
	global_load_dwordx4 v[6:9], v[2:3], off nt
	s_or_b32 s10, s28, 15
	s_mov_b32 s11, s15
	s_lshl_b64 s[26:27], s[10:11], 12
	v_lshl_add_u64 v[2:3], v[96:97], 0, s[26:27]
	s_waitcnt lgkmcnt(0)
	global_load_dwordx4 v[2:5], v[2:3], off nt
	s_lshl_b64 s[14:15], s[14:15], 11
	v_lshl_add_u64 v[98:99], v[94:95], 0, s[14:15]
	s_lshl_b64 s[14:15], s[16:17], 11
	v_lshl_add_u64 v[102:103], v[94:95], 0, s[14:15]
	s_lshl_b64 s[16:17], s[18:19], 11
	s_lshl_b64 s[18:19], s[20:21], 11
	s_lshl_b64 s[20:21], s[22:23], 11
	s_lshl_b64 s[22:23], s[24:25], 11
	v_lshl_add_u64 v[114:115], v[94:95], 0, s[16:17]
	s_lshl_b64 s[12:13], s[12:13], 11
	v_lshl_add_u64 v[116:117], v[94:95], 0, s[18:19]
	v_lshl_add_u64 v[118:119], v[94:95], 0, s[20:21]
	v_lshl_add_u64 v[120:121], v[94:95], 0, s[22:23]
	s_lshl_b64 s[10:11], s[10:11], 11
	s_waitcnt vmcnt(7)
	v_cvt_f16_f32_e32 v1, v110
	v_cvt_pk_f16_f32 v97, v111, v112
	v_cvt_f16_f32_e32 v100, v113
	v_pack_b32_f16 v122, v1, v97
	s_waitcnt vmcnt(6)
	v_cvt_f16_f32_e32 v124, v26
	v_cvt_f16_f32_e32 v1, v29
	v_mov_b32_e32 v96, v27
	v_cvt_pk_f16_f32 v27, v27, v28
	v_alignbit_b32 v123, v100, v97, 16
	global_store_dwordx2 v[98:99], v[122:123], off
	v_pack_b32_f16 v98, v124, v27
	v_alignbit_b32 v99, v1, v27, 16
	s_waitcnt vmcnt(6)
	v_cvt_f16_f32_e32 v97, v22
	v_cvt_pk_f16_f32 v100, v23, v24
	s_waitcnt vmcnt(5)
	v_cvt_f16_f32_e32 v123, v18
	v_cvt_f16_f32_e32 v27, v21
	v_cvt_pk_f16_f32 v1, v19, v20
	v_cvt_f16_f32_e32 v122, v25
	global_store_dwordx2 v[102:103], v[98:99], off
	v_pack_b32_f16 v98, v97, v100
	v_pack_b32_f16 v102, v123, v1
	v_alignbit_b32 v103, v27, v1, 16
	s_waitcnt vmcnt(5)
	v_cvt_f16_f32_e32 v124, v14
	v_cvt_f16_f32_e32 v126, v17
	s_waitcnt vmcnt(4)
	v_cvt_f16_f32_e32 v97, v10
	v_cvt_f16_f32_e32 v1, v13
	v_cvt_pk_f16_f32 v125, v15, v16
	v_cvt_pk_f16_f32 v27, v11, v12
	v_alignbit_b32 v99, v122, v100, 16
	v_pack_b32_f16 v122, v124, v125
	v_alignbit_b32 v123, v126, v125, 16
	v_pack_b32_f16 v124, v97, v27
	v_alignbit_b32 v125, v1, v27, 16
	s_waitcnt vmcnt(3)
	v_cvt_f16_f32_e32 v1, v6
	v_cvt_f16_f32_e32 v27, v9
	v_cvt_pk_f16_f32 v97, v7, v8
	global_store_dwordx2 v[114:115], v[98:99], off
	global_store_dwordx2 v[116:117], v[102:103], off
	global_store_dwordx2 v[118:119], v[122:123], off
	global_store_dwordx2 v[120:121], v[124:125], off
	v_pack_b32_f16 v98, v1, v97
	v_alignbit_b32 v99, v27, v97, 16
	v_lshl_add_u64 v[102:103], v[94:95], 0, s[12:13]
	global_store_dwordx2 v[102:103], v[98:99], off
	v_cvt_f64_f32_e32 v[102:103], v111
	v_cvt_f64_f32_e32 v[98:99], v110
	v_mul_f64 v[114:115], v[52:53], v[102:103]
	v_mul_f64 v[122:123], v[42:43], v[102:103]
	v_cvt_f64_f32_e32 v[110:111], v112
	v_fmac_f64_e32 v[114:115], v[48:49], v[98:99]
	v_fmac_f64_e32 v[122:123], v[36:37], v[98:99]
	v_cvt_f64_f32_e32 v[112:113], v113
	v_fmac_f64_e32 v[114:115], v[50:51], v[110:111]
	v_fmac_f64_e32 v[122:123], v[38:39], v[110:111]
	v_mul_f64 v[116:117], v[74:75], v[102:103]
	v_mul_f64 v[118:119], v[84:85], v[102:103]
	v_mul_f64 v[120:121], v[92:93], v[102:103]
	v_mul_f64 v[124:125], v[44:45], v[102:103]
	v_mul_f64 v[126:127], v[60:61], v[102:103]
	v_mul_f64 v[102:103], v[76:77], v[102:103]
	v_fmac_f64_e32 v[114:115], v[46:47], v[112:113]
	v_fmac_f64_e32 v[122:123], v[34:35], v[112:113]
	v_fmac_f64_e32 v[116:117], v[64:65], v[98:99]
	v_fmac_f64_e32 v[118:119], v[80:81], v[98:99]
	v_fmac_f64_e32 v[120:121], v[88:89], v[98:99]
	v_fmac_f64_e32 v[124:125], v[32:33], v[98:99]
	v_fmac_f64_e32 v[126:127], v[56:57], v[98:99]
	v_fmac_f64_e32 v[102:103], v[70:71], v[98:99]
	v_mov_b32_e32 v27, v28
	v_cndmask_b32_e32 v1, v115, v123, vcc
	v_cndmask_b32_e32 v28, v114, v122, vcc
	v_fmac_f64_e32 v[116:117], v[66:67], v[110:111]
	v_fmac_f64_e32 v[118:119], v[82:83], v[110:111]
	v_fmac_f64_e32 v[120:121], v[90:91], v[110:111]
	v_fmac_f64_e32 v[124:125], v[40:41], v[110:111]
	v_fmac_f64_e32 v[126:127], v[58:59], v[110:111]
	v_fmac_f64_e32 v[102:103], v[72:73], v[110:111]
	ds_bpermute_b32 v110, v101, v28
	ds_bpermute_b32 v111, v101, v1
	v_fmac_f64_e32 v[116:117], v[62:63], v[112:113]
	v_fmac_f64_e32 v[118:119], v[78:79], v[112:113]
	v_fmac_f64_e32 v[124:125], v[30:31], v[112:113]
	v_fmac_f64_e32 v[126:127], v[54:55], v[112:113]
	v_fmac_f64_e32 v[120:121], v[86:87], v[112:113]
	v_fmac_f64_e32 v[102:103], v[68:69], v[112:113]
	v_cndmask_b32_e32 v99, v123, v115, vcc
	v_cndmask_b32_e32 v98, v122, v114, vcc
	v_cndmask_b32_e32 v1, v117, v125, vcc
	v_cndmask_b32_e32 v97, v116, v124, vcc
	v_cndmask_b32_e32 v112, v124, v116, vcc
	v_cndmask_b32_e32 v100, v119, v127, vcc
	v_cndmask_b32_e32 v116, v118, v126, vcc
	v_cndmask_b32_e32 v113, v125, v117, vcc
	v_cndmask_b32_e32 v115, v127, v119, vcc
	v_cndmask_b32_e32 v114, v126, v118, vcc
	v_cndmask_b32_e32 v119, v121, v103, vcc
	v_cndmask_b32_e32 v118, v120, v102, vcc
	s_waitcnt lgkmcnt(0)
	v_add_f64 v[98:99], v[98:99], v[110:111]
	ds_bpermute_b32 v110, v101, v97
	ds_bpermute_b32 v111, v101, v1
	ds_bpermute_b32 v116, v101, v116
	ds_bpermute_b32 v117, v101, v100
	ds_bpermute_b32 v118, v101, v118
	ds_bpermute_b32 v119, v101, v119
	v_cndmask_b32_e32 v103, v103, v121, vcc
	v_cndmask_b32_e32 v102, v102, v120, vcc
	s_waitcnt lgkmcnt(4)
	v_add_f64 v[110:111], v[112:113], v[110:111]
	s_waitcnt lgkmcnt(2)
	v_add_f64 v[112:113], v[114:115], v[116:117]
	v_mov_b32_e32 v28, v23
	v_mov_b32_e32 v23, v24
	v_mov_b32_e32 v24, v19
	v_mov_b32_e32 v19, v20
	s_waitcnt lgkmcnt(0)
	v_add_f64 v[102:103], v[102:103], v[118:119]
	v_cndmask_b32_e64 v1, v99, v113, s[8:9]
	v_cndmask_b32_e64 v20, v98, v112, s[8:9]
	v_cndmask_b32_e64 v99, v113, v99, s[8:9]
	v_cndmask_b32_e64 v98, v112, v98, s[8:9]
	ds_bpermute_b32 v112, v104, v20
	ds_bpermute_b32 v113, v104, v1
	v_cndmask_b32_e64 v1, v111, v103, s[8:9]
	v_cndmask_b32_e64 v20, v110, v102, s[8:9]
	ds_bpermute_b32 v114, v104, v20
	ds_bpermute_b32 v115, v104, v1
	v_cndmask_b32_e64 v103, v103, v111, s[8:9]
	v_cndmask_b32_e64 v102, v102, v110, s[8:9]
	s_waitcnt lgkmcnt(2)
	v_add_f64 v[98:99], v[98:99], v[112:113]
	v_mov_b32_e32 v20, v15
	s_waitcnt lgkmcnt(0)
	v_add_f64 v[102:103], v[102:103], v[114:115]
	v_mov_b32_e32 v15, v16
	v_cndmask_b32_e64 v1, v99, v103, s[4:5]
	v_cndmask_b32_e64 v16, v98, v102, s[4:5]
	ds_bpermute_b32 v110, v105, v16
	ds_bpermute_b32 v111, v105, v1
	v_cndmask_b32_e64 v99, v103, v99, s[4:5]
	v_cndmask_b32_e64 v98, v102, v98, s[4:5]
	s_waitcnt vmcnt(7)
	v_cvt_f16_f32_e32 v1, v2
	v_cvt_f16_f32_e32 v16, v5
	s_waitcnt lgkmcnt(0)
	v_add_f64 v[98:99], v[98:99], v[110:111]
	ds_bpermute_b32 v102, v106, v98
	ds_bpermute_b32 v103, v106, v99
	v_cvt_pk_f16_f32 v97, v3, v4
	v_pack_b32_f16 v110, v1, v97
	v_alignbit_b32 v111, v16, v97, 16
	v_lshl_add_u64 v[94:95], v[94:95], 0, s[10:11]
	s_waitcnt lgkmcnt(0)
	v_add_f64 v[98:99], v[98:99], v[102:103]
	ds_bpermute_b32 v102, v107, v98
	ds_bpermute_b32 v103, v107, v99
	global_store_dwordx2 v[94:95], v[110:111], off
	v_mov_b32_e32 v16, v11
	v_mov_b32_e32 v11, v12
	v_mov_b32_e32 v12, v7
	s_waitcnt lgkmcnt(0)
	v_add_f64 v[94:95], v[98:99], v[102:103]
	ds_bpermute_b32 v98, v109, v94
	ds_bpermute_b32 v99, v109, v95
	v_mov_b32_e32 v7, v8
	v_mov_b32_e32 v8, v3
	v_mov_b32_e32 v1, v4
	s_and_saveexec_b64 s[10:11], s[6:7]
	s_cbranch_execz .LBB1_24
	s_waitcnt lgkmcnt(0)
	v_add_f64 v[94:95], v[94:95], v[98:99]
	ds_write_b64 v108, v[94:95] offset:2048

	.amdhsa_kernel _Z5k_prePKfS0_PiP15HIP_vector_typeIfLj2EES1_S0_S0_PDF16_S5_
		.amdhsa_group_segment_fixed_size 4096
		.amdhsa_private_segment_fixed_size 0
		.amdhsa_kernarg_size 72
		.amdhsa_user_sgpr_count 2
		.amdhsa_user_sgpr_dispatch_ptr 0
		.amdhsa_user_sgpr_queue_ptr 0
		.amdhsa_user_sgpr_kernarg_segment_ptr 1
		.amdhsa_user_sgpr_dispatch_id 0
		.amdhsa_user_sgpr_kernarg_preload_length 0
		.amdhsa_user_sgpr_kernarg_preload_offset 0
		.amdhsa_user_sgpr_private_segment_size 0
		.amdhsa_uses_dynamic_stack 0
		.amdhsa_enable_private_segment 0
		.amdhsa_system_sgpr_workgroup_id_x 1
		.amdhsa_system_sgpr_workgroup_id_y 0
		.amdhsa_system_sgpr_workgroup_id_z 0
		.amdhsa_system_sgpr_workgroup_info 0
		.amdhsa_system_vgpr_workitem_id 0
		.amdhsa_next_free_vgpr 128
		.amdhsa_next_free_sgpr 36
		.amdhsa_accum_offset 128
		.amdhsa_reserve_vcc 1
		.amdhsa_float_round_mode_32 0
		.amdhsa_float_round_mode_16_64 0
		.amdhsa_float_denorm_mode_32 3
		.amdhsa_float_denorm_mode_16_64 3
		.amdhsa_dx10_clamp 1
		.amdhsa_ieee_mode 1
		.amdhsa_fp16_overflow 0
		.amdhsa_tg_split 0
		.amdhsa_exception_fp_ieee_invalid_op 0
		.amdhsa_exception_fp_denorm_src 0
		.amdhsa_exception_fp_ieee_div_zero 0
		.amdhsa_exception_fp_ieee_overflow 0
		.amdhsa_exception_fp_ieee_underflow 0
		.amdhsa_exception_fp_ieee_inexact 0
		.amdhsa_exception_int_div_zero 0
	.end_amdhsa_kernel

amdhsa.kernels:
  - .agpr_count:     0
    .args:
      - .actual_access:  read_only
        .address_space:  global
        .offset:         0
        .size:           8
        .value_kind:     global_buffer
      - .actual_access:  read_only
        .address_space:  global
        .offset:         8
        .size:           8
        .value_kind:     global_buffer
      - .actual_access:  write_only
        .address_space:  global
        .offset:         16
        .size:           8
        .value_kind:     global_buffer
      - .actual_access:  write_only
        .address_space:  global
        .offset:         24
        .size:           8
        .value_kind:     global_buffer
      - .actual_access:  write_only
        .address_space:  global
        .offset:         32
        .size:           8
        .value_kind:     global_buffer
      - .actual_access:  write_only
        .address_space:  global
        .offset:         40
        .size:           8
        .value_kind:     global_buffer
    .group_segment_fixed_size: 256
    .kernarg_segment_align: 8
    .kernarg_segment_size: 48
    .language:       OpenCL C
    .language_version:
      - 2
      - 0
    .max_flat_workgroup_size: 256
    .name:           _Z10k_xscatterPKiS0_P15HIP_vector_typeIiLj2EEPtP4MetaS3_
    .private_segment_fixed_size: 0
    .sgpr_count:     41
    .sgpr_spill_count: 0
    .symbol:         _Z10k_xscatterPKiS0_P15HIP_vector_typeIiLj2EEPtP4MetaS3_.kd
    .uniform_work_group_size: 1
    .uses_dynamic_stack: false
    .vgpr_count:     55
    .vgpr_spill_count: 0
    .wavefront_size: 64
  - .agpr_count:     0
    .args:
      - .actual_access:  read_only
        .address_space:  global
        .offset:         0
        .size:           8
        .value_kind:     global_buffer
      - .actual_access:  read_only
        .address_space:  global
        .offset:         8
        .size:           8
        .value_kind:     global_buffer
      - .actual_access:  write_only
        .address_space:  global
        .offset:         16
        .size:           8
        .value_kind:     global_buffer
      - .actual_access:  write_only
        .address_space:  global
        .offset:         24
        .size:           8
        .value_kind:     global_buffer
      - .actual_access:  write_only
        .address_space:  global
        .offset:         32
        .size:           8
        .value_kind:     global_buffer
      - .actual_access:  read_only
        .address_space:  global
        .offset:         40
        .size:           8
        .value_kind:     global_buffer
      - .actual_access:  read_only
        .address_space:  global
        .offset:         48
        .size:           8
        .value_kind:     global_buffer
      - .actual_access:  write_only
        .address_space:  global
        .offset:         56
        .size:           8
        .value_kind:     global_buffer
      - .actual_access:  write_only
        .address_space:  global
        .offset:         64
        .size:           8
        .value_kind:     global_buffer
    .group_segment_fixed_size: 4096
    .kernarg_segment_align: 8
    .kernarg_segment_size: 72
    .language:       OpenCL C
    .language_version:
      - 2
      - 0
    .max_flat_workgroup_size: 256
    .name:           _Z5k_prePKfS0_PiP15HIP_vector_typeIfLj2EES1_S0_S0_PDF16_S5_
    .private_segment_fixed_size: 0
    .sgpr_count:     42
    .sgpr_spill_count: 0
    .symbol:         _Z5k_prePKfS0_PiP15HIP_vector_typeIfLj2EES1_S0_S0_PDF16_S5_.kd
    .uniform_work_group_size: 1
    .uses_dynamic_stack: false
    .vgpr_count:     128
    .vgpr_spill_count: 0
    .wavefront_size: 64
  - .agpr_count:     0
    .args:
      - .address_space:  global
        .offset:         0
        .size:           8
        .value_kind:     global_buffer
      - .address_space:  global
        .offset:         8
        .size:           8
        .value_kind:     global_buffer
      - .actual_access:  write_only
        .address_space:  global
        .offset:         16
        .size:           8
        .value_kind:     global_buffer
      - .actual_access:  read_only
        .address_space:  global
        .offset:         24
        .size:           8
        .value_kind:     global_buffer
    .group_segment_fixed_size: 0
    .kernarg_segment_align: 8
    .kernarg_segment_size: 32
    .language:       OpenCL C
    .language_version:
      - 2
      - 0
    .max_flat_workgroup_size: 512
    .name:           _Z7k_gemm2PKDF16_S0_PDF16_PK15HIP_vector_typeIiLj2EE
    .private_segment_fixed_size: 0
    .sgpr_count:     74
    .sgpr_spill_count: 0
    .symbol:         _Z7k_gemm2PKDF16_S0_PDF16_PK15HIP_vector_typeIiLj2EE.kd
    .uniform_work_group_size: 1
    .uses_dynamic_stack: false
    .vgpr_count:     226
    .vgpr_spill_count: 0
    .wavefront_size: 64
  - .agpr_count:     0
    .args:
      - .actual_access:  read_only
        .address_space:  global
        .offset:         0
        .size:           8
        .value_kind:     global_buffer
      - .actual_access:  read_only
        .address_space:  global
        .offset:         8
        .size:           8
        .value_kind:     global_buffer
      - .actual_access:  read_only
        .address_space:  global
        .offset:         16
        .size:           8
        .value_kind:     global_buffer
      - .actual_access:  write_only
        .address_space:  global
        .offset:         24
        .size:           8
        .value_kind:     global_buffer
    .group_segment_fixed_size: 0
    .kernarg_segment_align: 8
    .kernarg_segment_size: 32
    .language:       OpenCL C
    .language_version:
      - 2
      - 0
    .max_flat_workgroup_size: 256
    .name:           _Z9k_combinePKDF16_PK15HIP_vector_typeIiLj2EEPKS1_IfLj2EEPf
    .private_segment_fixed_size: 0
    .sgpr_count:     30
    .sgpr_spill_count: 0
    .symbol:         _Z9k_combinePKDF16_PK15HIP_vector_typeIiLj2EEPKS1_IfLj2EEPf.kd
    .uniform_work_group_size: 1
    .uses_dynamic_stack: false
    .vgpr_count:     64
    .vgpr_spill_count: 0
    .wavefront_size: 64
  - .agpr_count:     0
    .args:
      - .address_space:  global
        .offset:         0
        .size:           8
        .value_kind:     global_buffer
      - .address_space:  global
        .offset:         8
        .size:           8
        .value_kind:     global_buffer
      - .actual_access:  write_only
        .address_space:  global
        .offset:         16
        .size:           8
        .value_kind:     global_buffer
      - .actual_access:  read_only
        .address_space:  global
        .offset:         24
        .size:           8
        .value_kind:     global_buffer
      - .address_space:  global
        .offset:         32
        .size:           8
        .value_kind:     global_buffer
      - .address_space:  global
        .offset:         40
        .size:           8
        .value_kind:     global_buffer
      - .actual_access:  write_only
        .address_space:  global
        .offset:         48
        .size:           8
        .value_kind:     global_buffer
      - .address_space:  global
        .offset:         56
        .size:           8
        .value_kind:     global_buffer
    .group_segment_fixed_size: 0
    .kernarg_segment_align: 8
    .kernarg_segment_size: 64
    .language:       OpenCL C
    .language_version:
      - 2
      - 0
    .max_flat_workgroup_size: 512
    .name:           _Z7k_gemm1ILi0EEvPKDF16_S1_PDF16_PK15HIP_vector_typeIiLj2EEPKfS8_S2_PKt
    .private_segment_fixed_size: 0
    .sgpr_count:     106
    .sgpr_spill_count: 0
    .symbol:         _Z7k_gemm1ILi0EEvPKDF16_S1_PDF16_PK15HIP_vector_typeIiLj2EEPKfS8_S2_PKt.kd
    .uniform_work_group_size: 1
    .uses_dynamic_stack: false
    .vgpr_count:     256
    .vgpr_spill_count: 0
    .wavefront_size: 64
  - .agpr_count:     0
    .args:
      - .address_space:  global
        .offset:         0
        .size:           8
        .value_kind:     global_buffer
      - .address_space:  global
        .offset:         8
        .size:           8
        .value_kind:     global_buffer
      - .actual_access:  write_only
        .address_space:  global
        .offset:         16
        .size:           8
        .value_kind:     global_buffer
      - .actual_access:  read_only
        .address_space:  global
        .offset:         24
        .size:           8
        .value_kind:     global_buffer
      - .address_space:  global
        .offset:         32
        .size:           8
        .value_kind:     global_buffer
      - .actual_access:  read_only
        .address_space:  global
        .offset:         40
        .size:           8
        .value_kind:     global_buffer
      - .actual_access:  write_only
        .address_space:  global
        .offset:         48
        .size:           8
        .value_kind:     global_buffer
      - .address_space:  global
        .offset:         56
        .size:           8
        .value_kind:     global_buffer
    .group_segment_fixed_size: 0
    .kernarg_segment_align: 8
    .kernarg_segment_size: 64
    .language:       OpenCL C
    .language_version:
      - 2
      - 0
    .max_flat_workgroup_size: 512
    .name:           _Z7k_gemm1ILi1EEvPKDF16_S1_PDF16_PK15HIP_vector_typeIiLj2EEPKfS8_S2_PKt
    .private_segment_fixed_size: 0
    .sgpr_count:     96
    .sgpr_spill_count: 0
    .symbol:         _Z7k_gemm1ILi1EEvPKDF16_S1_PDF16_PK15HIP_vector_typeIiLj2EEPKfS8_S2_PKt.kd
    .uniform_work_group_size: 1
    .uses_dynamic_stack: false
    .vgpr_count:     254
    .vgpr_spill_count: 0
    .wavefront_size: 64
